# baseline (speedup 1.0000x reference)
_Z9ssim_mainPKfS0_S0_Pf:
	v_readfirstlane_b32 s29, v0
	s_load_dwordx4 s[4:7], s[0:1], 0x0
	s_load_dwordx4 s[8:11], s[0:1], 0x10
	s_mov_b32 s51, 0x44800000
	s_mov_b32 s38, 0
	s_mov_b32 s39, -1
	s_lshr_b32 s12, s29, 6
	s_cmp_lt_u32 s12, 4
	s_cbranch_scc1 .Lq_noprio0
	s_setprio 1
.Lq_noprio0:
	s_mov_b32 s13, s2
	s_lshr_b32 s14, s13, 3
	s_and_b32 s15, s13, 7
	s_lshl_b32 s16, s14, 20
	s_lshl_b32 s17, s15, 17
	s_add_u32 s16, s16, s17
	s_lshl_b32 s17, s12, 8
	s_add_u32 s16, s16, s17
	s_lshl_b32 s27, s12, 2
	s_add_u32 s27, s27, 0x10000
	v_and_b32_e32 v8, 63, v0
	v_and_b32_e32 v169, 15, v0
	v_bfe_u32 v164, v0, 4, 2
	v_lshrrev_b32_e32 v167, 2, v169
	v_lshlrev_b32_e32 v167, 5, v167
	v_and_b32_e32 v168, 1, v169
	v_lshl_or_b32 v167, v168, 4, v167
	v_bfe_u32 v168, v169, 1, 1
	v_lshl_or_b32 v167, v168, 7, v167
	v_lshl_or_b32 v9, v164, 14, v167
	v_and_b32_e32 v168, 1, v164
	v_lshl_or_b32 v23, v168, 14, v167
	v_lshrrev_b32_e32 v168, 1, v164
	v_lshl_or_b32 v23, v168, 13, v23
	v_add_u32_e32 v237, 0x1000, v9
	v_add_u32_e32 v238, 0x2000, v9
	v_add_u32_e32 v239, 0x3000, v9
	v_add_u32_e32 v240, 0x10000, v9
	v_add_u32_e32 v241, 0x11000, v9
	v_add_u32_e32 v242, 0x12000, v9
	v_add_u32_e32 v243, 0x13000, v9
	s_waitcnt lgkmcnt(0)
	s_load_dwordx8 s[40:47], s[8:9], 0x0
	s_load_dwordx2 s[48:49], s[8:9], 0x20
	s_load_dword s50, s[8:9], 0x28
	s_add_u32 s18, s4, s16
	s_addc_u32 s19, s5, 0
	s_add_u32 s20, s6, s16
	s_addc_u32 s21, s7, 0
	global_load_dwordx4 v[36:39], v9, s[18:19] offset:0 sc1 nt
	global_load_dwordx4 v[40:43], v9, s[18:19] offset:2048 sc1 nt
	global_load_dwordx4 v[68:71], v9, s[20:21] offset:0 sc1 nt
	global_load_dwordx4 v[72:75], v9, s[20:21] offset:2048 sc1 nt
	global_load_dwordx4 v[44:47], v237, s[18:19] offset:0 sc1 nt
	global_load_dwordx4 v[48:51], v237, s[18:19] offset:2048 sc1 nt
	global_load_dwordx4 v[76:79], v237, s[20:21] offset:0 sc1 nt
	global_load_dwordx4 v[80:83], v237, s[20:21] offset:2048 sc1 nt
	global_load_dwordx4 v[52:55], v238, s[18:19] offset:0 sc1 nt
	global_load_dwordx4 v[56:59], v238, s[18:19] offset:2048 sc1 nt
	global_load_dwordx4 v[84:87], v238, s[20:21] offset:0 sc1 nt
	global_load_dwordx4 v[88:91], v238, s[20:21] offset:2048 sc1 nt
	global_load_dwordx4 v[60:63], v239, s[18:19] offset:0 sc1 nt
	global_load_dwordx4 v[64:67], v239, s[18:19] offset:2048 sc1 nt
	global_load_dwordx4 v[92:95], v239, s[20:21] offset:0 sc1 nt
	global_load_dwordx4 v[96:99], v239, s[20:21] offset:2048 sc1 nt
	v_mov_b32_e32 v6, s27
	v_mov_b32_e32 v168, 0
	ds_write_b32 v6, v168 offset:0
	ds_write_b32 v6, v168 offset:32
	ds_write_b32 v6, v168 offset:64
	ds_write_b32 v6, v168 offset:96
	v_lshlrev_b32_e32 v167, 3, v164
	v_xor_b32_e32 v168, 16, v167
	v_sub_u32_e32 v165, v167, v169
	v_sub_u32_e32 v166, v168, v169
	v_add_u32_e32 v172, 0, v165
	v_min_u32_e32 v172, 11, v172
	v_lshlrev_b32_e32 v172, 2, v172
	v_add_u32_e32 v173, 1, v165
	v_min_u32_e32 v173, 11, v173
	v_lshlrev_b32_e32 v173, 2, v173
	v_add_u32_e32 v174, 2, v165
	v_min_u32_e32 v174, 11, v174
	v_lshlrev_b32_e32 v174, 2, v174
	v_add_u32_e32 v175, 3, v165
	v_min_u32_e32 v175, 11, v175
	v_lshlrev_b32_e32 v175, 2, v175
	v_add_u32_e32 v176, 4, v165
	v_min_u32_e32 v176, 11, v176
	v_lshlrev_b32_e32 v176, 2, v176
	v_add_u32_e32 v177, 5, v165
	v_min_u32_e32 v177, 11, v177
	v_lshlrev_b32_e32 v177, 2, v177
	v_add_u32_e32 v178, 6, v165
	v_min_u32_e32 v178, 11, v178
	v_lshlrev_b32_e32 v178, 2, v178
	v_add_u32_e32 v179, 7, v165
	v_min_u32_e32 v179, 11, v179
	v_lshlrev_b32_e32 v179, 2, v179
	v_add_u32_e32 v180, 0, v166
	v_min_u32_e32 v180, 11, v180
	v_lshlrev_b32_e32 v180, 2, v180
	v_add_u32_e32 v181, 1, v166
	v_min_u32_e32 v181, 11, v181
	v_lshlrev_b32_e32 v181, 2, v181
	v_add_u32_e32 v182, 2, v166
	v_min_u32_e32 v182, 11, v182
	v_lshlrev_b32_e32 v182, 2, v182
	v_add_u32_e32 v183, 3, v166
	v_min_u32_e32 v183, 11, v183
	v_lshlrev_b32_e32 v183, 2, v183
	v_add_u32_e32 v184, 4, v166
	v_min_u32_e32 v184, 11, v184
	v_lshlrev_b32_e32 v184, 2, v184
	v_add_u32_e32 v185, 5, v166
	v_min_u32_e32 v185, 11, v185
	v_lshlrev_b32_e32 v185, 2, v185
	v_add_u32_e32 v186, 6, v166
	v_min_u32_e32 v186, 11, v186
	v_lshlrev_b32_e32 v186, 2, v186
	v_add_u32_e32 v187, 7, v166
	v_min_u32_e32 v187, 11, v187
	v_lshlrev_b32_e32 v187, 2, v187
	s_cmp_eq_u32 s15, 7
	s_cselect_b32 s22, 0, 0x20000
	s_add_u32 s84, s18, s22
	s_addc_u32 s85, s19, 0
	s_add_u32 s86, s18, s22
	s_addc_u32 s87, s19, 0
	s_add_u32 s86, s86, 0x1000
	s_addc_u32 s87, s87, 0
	s_add_u32 s88, s20, s22
	s_addc_u32 s89, s21, 0
	s_add_u32 s90, s20, s22
	s_addc_u32 s91, s21, 0
	s_add_u32 s90, s90, 0x1000
	s_addc_u32 s91, s91, 0
	s_waitcnt lgkmcnt(0)
	v_writelane_b32 v171, s40, 0
	v_writelane_b32 v171, s41, 1
	v_writelane_b32 v171, s42, 2
	v_writelane_b32 v171, s43, 3
	v_writelane_b32 v171, s44, 4
	v_writelane_b32 v171, s45, 5
	v_writelane_b32 v171, s46, 6
	v_writelane_b32 v171, s47, 7
	v_writelane_b32 v171, s48, 8
	v_writelane_b32 v171, s49, 9
	v_writelane_b32 v171, s50, 10
	v_writelane_b32 v171, 0, 11
	v_fma_mixlo_f16 v171, v171, s51, 0
	ds_bpermute_b32 v188, v172, v171
	ds_bpermute_b32 v189, v173, v171
	ds_bpermute_b32 v190, v174, v171
	ds_bpermute_b32 v191, v175, v171
	ds_bpermute_b32 v192, v176, v171
	ds_bpermute_b32 v193, v177, v171
	ds_bpermute_b32 v194, v178, v171
	ds_bpermute_b32 v195, v179, v171
	v_mov_b32_e32 v229, 0x44800000
	v_fma_mixlo_f16 v228, s40, v229, 0
	v_cvt_f32_f16_e32 v228, v228
	v_cvt_f64_f32_e32 v[212:213], v228
	v_add_f64 v[212:213], v[212:213], 0
	v_fma_mixlo_f16 v228, s41, v229, 0
	v_cvt_f32_f16_e32 v228, v228
	v_cvt_f64_f32_e32 v[214:215], v228
	v_add_f64 v[212:213], v[212:213], v[214:215]
	v_fma_mixlo_f16 v228, s42, v229, 0
	v_cvt_f32_f16_e32 v228, v228
	v_cvt_f64_f32_e32 v[214:215], v228
	v_add_f64 v[212:213], v[212:213], v[214:215]
	v_fma_mixlo_f16 v228, s43, v229, 0
	v_cvt_f32_f16_e32 v228, v228
	v_cvt_f64_f32_e32 v[214:215], v228
	v_add_f64 v[212:213], v[212:213], v[214:215]
	v_fma_mixlo_f16 v228, s44, v229, 0
	v_cvt_f32_f16_e32 v228, v228
	v_cvt_f64_f32_e32 v[214:215], v228
	v_add_f64 v[212:213], v[212:213], v[214:215]
	v_fma_mixlo_f16 v228, s45, v229, 0
	v_cvt_f32_f16_e32 v228, v228
	v_cvt_f64_f32_e32 v[214:215], v228
	v_add_f64 v[212:213], v[212:213], v[214:215]
	v_fma_mixlo_f16 v228, s46, v229, 0
	v_cvt_f32_f16_e32 v228, v228
	v_cvt_f64_f32_e32 v[214:215], v228
	v_add_f64 v[212:213], v[212:213], v[214:215]
	v_fma_mixlo_f16 v228, s47, v229, 0
	v_cvt_f32_f16_e32 v228, v228
	v_cvt_f64_f32_e32 v[214:215], v228
	v_add_f64 v[212:213], v[212:213], v[214:215]
	v_fma_mixlo_f16 v228, s48, v229, 0
	v_cvt_f32_f16_e32 v228, v228
	v_cvt_f64_f32_e32 v[214:215], v228
	v_add_f64 v[212:213], v[212:213], v[214:215]
	v_fma_mixlo_f16 v228, s49, v229, 0
	v_cvt_f32_f16_e32 v228, v228
	v_cvt_f64_f32_e32 v[214:215], v228
	v_add_f64 v[212:213], v[212:213], v[214:215]
	v_fma_mixlo_f16 v228, s50, v229, 0
	v_cvt_f32_f16_e32 v228, v228
	v_cvt_f64_f32_e32 v[214:215], v228
	v_add_f64 v[212:213], v[212:213], v[214:215]
	s_waitcnt lgkmcnt(7)
	ds_bpermute_b32 v196, v180, v171
	ds_bpermute_b32 v197, v181, v171
	ds_bpermute_b32 v198, v182, v171
	ds_bpermute_b32 v199, v183, v171
	ds_bpermute_b32 v200, v184, v171
	ds_bpermute_b32 v201, v185, v171
	ds_bpermute_b32 v202, v186, v171
	ds_bpermute_b32 v203, v187, v171
	v_mul_f64 v[212:213], v[212:213], v[212:213]
	v_mul_f64 v[216:217], v[212:213], 0.5
	v_add_f64 v[218:219], v[216:217], v[216:217]
	s_mov_b32 s36, 0xeb1c432d
	s_mov_b32 s37, 0x3f1a36e2
	v_mul_f64 v[220:221], v[212:213], s[36:37]
	v_mul_f64 v[222:223], v[216:217], v[218:219]
	v_fmac_f64_e32 v[222:223], v[212:213], v[220:221]
	v_add_f64 v[224:225], v[212:213], v[212:213]
	s_mov_b32 s36, 0x487fcb92
	s_mov_b32 s37, 0x3f4d7dbf
	v_mul_f64 v[226:227], v[212:213], s[36:37]
	v_cvt_f32_f64_e32 v0, v[226:227]
	v_mov_b32_e32 v1, v0
	v_mov_b32_e32 v2, v0
	v_mov_b32_e32 v3, v0
	v_cvt_f32_f64_e32 v10, v[218:219]
	v_cvt_f32_f64_e32 v11, v[222:223]
	v_cvt_f32_f64_e32 v12, v[212:213]
	v_cvt_f32_f64_e32 v13, v[224:225]
	v_mul_f64 v[226:227], v[212:213], v[226:227]
	v_cvt_f32_f64_e32 v14, v[226:227]
	v_lshlrev_b32_e32 v167, 2, v164
	s_cmp_eq_u32 s12, 0
	s_cselect_b32 s23, 6, 64
	v_add_u32_e32 v168, 0, v167
	v_cmp_gt_u32_e32 vcc, s23, v168
	s_nop 1
	v_cndmask_b32_e64 v15, 0, 1.0, vcc
	v_add_u32_e32 v168, 1, v167
	v_cmp_gt_u32_e32 vcc, s23, v168
	s_nop 1
	v_cndmask_b32_e64 v16, 0, 1.0, vcc
	v_add_u32_e32 v168, 2, v167
	v_cmp_gt_u32_e32 vcc, s23, v168
	s_nop 1
	v_cndmask_b32_e64 v17, 0, 1.0, vcc
	v_add_u32_e32 v168, 3, v167
	v_cmp_gt_u32_e32 vcc, s23, v168
	s_nop 1
	v_cndmask_b32_e64 v18, 0, 1.0, vcc
	v_and_b32_e32 v167, 31, v8
	v_lshlrev_b32_e32 v167, 4, v167
	s_lshl_b32 s24, s12, 11
	s_add_i32 s25, s12, 7
	s_and_b32 s25, s25, 7
	s_lshl_b32 s26, s25, 11
	v_or_b32_e32 v4, s24, v167
	v_or_b32_e32 v5, s26, v167
	s_lshl_b32 s28, s25, 2
	s_add_u32 s28, s28, 0x10000
	v_mov_b32_e32 v7, s28
	v_mov_b32_e32 v19, 0
	v_mov_b32_e32 v20, 0
	v_mov_b32_e32 v21, 0
	v_mov_b32_e32 v22, 0
	s_waitcnt lgkmcnt(0)
	v_cmp_lt_u32_e64 s[32:33], 31, v8
	v_cmp_gt_u32_e64 s[34:35], 32, v8
	v_pack_b32_f16 v24, v188, v189
	v_pack_b32_f16 v25, v190, v191
	v_pack_b32_f16 v26, v192, v193
	v_pack_b32_f16 v27, v194, v195
	v_pack_b32_f16 v167, v196, v197
	v_cndmask_b32_e64 v28, 0, v167, s[32:33]
	v_cndmask_b32_e64 v32, 0, v167, s[34:35]
	v_pack_b32_f16 v167, v198, v199
	v_cndmask_b32_e64 v29, 0, v167, s[32:33]
	v_cndmask_b32_e64 v33, 0, v167, s[34:35]
	v_pack_b32_f16 v167, v200, v201
	v_cndmask_b32_e64 v30, 0, v167, s[32:33]
	v_cndmask_b32_e64 v34, 0, v167, s[34:35]
	v_pack_b32_f16 v167, v202, v203
	v_cndmask_b32_e64 v31, 0, v167, s[32:33]
	v_cndmask_b32_e64 v35, 0, v167, s[34:35]
	s_waitcnt lgkmcnt(0)
	s_barrier
	s_cmp_lt_u32 s12, 4
	s_cbranch_scc1 .Lq_noprio
	s_setprio 1
